# prio + PREP1 remap + NA bias fix + L0 attention idle workgroups convert 12 instead of 9 tiles per wave
# speedup vs baseline: 1.0039x; 1.0039x over previous
.LBB0_643:
	s_not_b32 s0, s41
	s_add_i32 s42, s46, s0
	s_mov_b64 s[0:1], -1
	s_cmpk_gt_i32 s42, 0x87
	s_waitcnt vmcnt(0)
	v_lshlrev_b32_e32 v172, 2, v184
	s_cbranch_scc0 .LBB0_720
	s_ashr_i32 s0, s47, 6
	s_lshl_b32 s1, s41, 3
	s_add_i32 s40, s1, s0
	s_add_u32 s41, s6, 0x17458000
	s_mulk_i32 s0, 0x2400
	s_addc_u32 s43, s7, 0
	s_add_i32 s0, s0, 0
	s_add_u32 s44, s6, 0x7458000
	s_addc_u32 s45, s7, 0
	s_add_u32 s47, s6, 0x6458000
	s_addc_u32 s48, s7, 0
	s_add_u32 s49, s6, 0x5458000
	s_addc_u32 s50, s7, 0
	s_add_u32 s51, s6, 0x4d58000
	s_addc_u32 s52, s7, 0
	s_add_u32 s53, s6, 0x158000
	s_addc_u32 s54, s7, 0
	s_add_u32 s55, s6, 0x3390c000
	v_lshlrev_b32_e32 v2, 4, v184
	s_addc_u32 s56, s7, 0
	v_lshlrev_b32_e32 v0, 2, v184
	v_and_b32_e32 v78, 48, v2
	s_add_u32 s57, s6, 0x35e0c000
	v_lshlrev_b32_e32 v2, 1, v184
	v_and_b32_e32 v82, 48, v184
	v_and_b32_e32 v0, 60, v0
	v_bfe_u32 v83, v184, 2, 4
	s_addc_u32 s58, s7, 0
	v_and_b32_e32 v2, 0x60, v2
	v_and_b32_e32 v8, 7, v184
	v_bfe_u32 v87, v184, 3, 3
	v_mov_b32_e32 v77, 0
	v_add_u32_e32 v1, s0, v82
	v_mul_u32_u24_e32 v3, 0x50, v0
	v_add_u32_e32 v4, s0, v78
	v_mul_u32_u24_e32 v5, 0x50, v83
	s_add_u32 s59, s6, 0x3760c000
	v_add_u32_e32 v6, s0, v2
	v_mul_u32_u24_e32 v7, 0x90, v0
	v_lshlrev_b32_e32 v2, 3, v8
	v_lshl_add_u32 v8, v8, 4, s0
	v_mul_u32_u24_e32 v9, 0x90, v87
	s_mul_i32 s40, s40, 12
	s_mov_b32 s1, 0
	v_mov_b32_e32 v79, v77
	v_or_b32_e32 v84, 16, v83
	v_or_b32_e32 v85, 32, v83
	v_or_b32_e32 v86, 48, v83
	s_addc_u32 s60, s7, 0
	v_or_b32_e32 v88, 8, v87
	v_or_b32_e32 v89, 16, v87
	v_or_b32_e32 v90, 24, v87
	v_or_b32_e32 v91, 32, v87
	v_or_b32_e32 v92, 40, v87
	v_or_b32_e32 v93, 48, v87
	v_or_b32_e32 v94, 56, v87
	s_mov_b32 s65, -12
	s_addk_i32 s40, 3
	s_add_i32 s61, 0, 0x204f8
	s_movk_i32 s62, 0x2000
	s_movk_i32 s63, 0x4000
	s_movk_i32 s64, 0x6000
	s_mov_b32 s66, 0x12000
	s_mov_b32 s67, 0xc3e00000
	v_add_u32_e32 v95, v1, v3
	v_add_u32_e32 v96, v4, v5
	s_movk_i32 s68, 0x3000
	s_movk_i32 s69, 0x5000
	s_movk_i32 s70, 0x7000
	s_add_i32 s71, 0, 0x204c0
	s_add_i32 s72, 0, 0x204b8
	s_add_i32 s73, 0, 0x204b0
	s_add_i32 s74, 0, 0x204a8
	s_add_i32 s75, 0, 0x20458
	s_add_i32 s76, 0, 0x20448
	s_add_i32 s77, 0, 0x20440
	s_mov_b32 s78, 0x9000
	s_mov_b32 s79, 0x1b000
	s_mov_b32 s80, 0x25000
	s_mov_b32 s81, 0x2e000
	s_mov_b32 s82, 0x37000
	s_mov_b32 s83, 0x41000
	s_mov_b32 s84, 0x4a000
	s_mov_b32 s85, 0x53000
	s_mov_b32 s86, 0x5d000
	s_mov_b32 s87, 0x66000
	s_mov_b32 s88, 0x6f000
	s_mov_b32 s89, 0x79000
	s_mov_b32 s90, 0x82000
	s_mov_b32 s91, 0x8b000
	v_add_u32_e32 v97, v6, v7
	v_lshlrev_b32_e32 v76, 1, v2
	v_lshlrev_b32_e32 v80, 2, v0
	v_mov_b32_e32 v98, 0x43e00000
	v_mov_b32_e32 v100, v77
	v_mov_b32_e32 v101, v77
	v_mov_b32_e32 v102, v77
	v_mov_b32_e32 v103, v77
	v_add_u32_e32 v99, v8, v9
	s_branch .LBB0_647

.LBB0_1058:
	s_add_i32 s1, s40, 0xffffff78
	s_lshl_b32 s0, s38, 3
	s_max_i32 s1, s1, 0
	s_mulk_i32 s1, 96
	s_add_i32 s0, s42, s0
	s_add_i32 s43, s0, s1
	s_cmpk_gt_i32 s43, 0x5fff
	s_mov_b32 s1, 0
	s_cbranch_scc1 .LBB0_1135
	s_lshl_b32 s44, s40, 3
	s_add_u32 s45, s10, 0x17458000
	s_mul_i32 s0, s42, 0x2400
	s_addc_u32 s46, s11, 0
	s_add_i32 s0, s0, 0
	s_add_u32 s47, s10, 0x7458000
	s_addc_u32 s48, s11, 0
	s_add_u32 s49, s10, 0x6458000
	s_addc_u32 s50, s11, 0
	s_add_u32 s51, s10, 0x5458000
	s_addc_u32 s52, s11, 0
	s_add_u32 s53, s10, 0x4d58000
	s_addc_u32 s54, s11, 0
	s_add_u32 s55, s10, 0x158000
	s_addc_u32 s56, s11, 0
	s_add_u32 s57, s10, 0x3390c000
	s_addc_u32 s58, s11, 0
	s_add_u32 s59, s10, 0x35e0c000
	v_lshlrev_b32_e32 v2, 1, v86
	v_and_b32_e32 v0, 60, v0
	v_and_b32_e32 v80, 48, v54
	s_addc_u32 s60, s11, 0
	v_and_b32_e32 v2, 0x60, v2
	v_and_b32_e32 v8, 7, v85
	v_lshrrev_b32_e32 v90, 3, v86
	v_mov_b32_e32 v79, 0
	v_add_u32_e32 v1, s0, v76
	v_mul_u32_u24_e32 v3, 0x50, v0
	v_add_u32_e32 v4, s0, v80
	v_mul_u32_u24_e32 v5, 0x50, v87
	s_add_u32 s61, s10, 0x3760c000
	v_add_u32_e32 v6, s0, v2
	v_mul_u32_u24_e32 v7, 0x90, v0
	v_lshlrev_b32_e32 v2, 3, v8
	v_lshl_add_u32 v8, v8, 4, s0
	v_mul_u32_u24_e32 v9, 0x90, v90
	v_mov_b32_e32 v81, v79
	v_or_b32_e32 v77, 16, v87
	v_or_b32_e32 v88, 32, v87
	v_or_b32_e32 v89, 48, v87
	s_addc_u32 s62, s11, 0
	v_or_b32_e32 v91, 8, v90
	v_or_b32_e32 v92, 16, v90
	v_or_b32_e32 v93, 24, v90
	v_or_b32_e32 v94, 32, v90
	v_or_b32_e32 v95, 40, v90
	v_or_b32_e32 v96, 48, v90
	v_or_b32_e32 v97, 56, v90
	s_add_i32 s63, 0, 0x204f8
	s_movk_i32 s64, 0x2000
	s_movk_i32 s65, 0x4000
	s_movk_i32 s66, 0x6000
	s_mov_b32 s67, 0x12000
	s_mov_b32 s68, 0xc3e00000
	v_add_u32_e32 v98, v1, v3
	v_add_u32_e32 v99, v4, v5
	s_movk_i32 s69, 0x3000
	s_movk_i32 s70, 0x5000
	s_movk_i32 s71, 0x7000
	s_add_i32 s72, 0, 0x204c0
	s_add_i32 s73, 0, 0x204b8
	s_add_i32 s74, 0, 0x204b0
	s_add_i32 s75, 0, 0x204a8
	s_add_i32 s76, 0, 0x20458
	s_add_i32 s77, 0, 0x20448
	s_add_i32 s78, 0, 0x20440
	s_mov_b32 s79, 0x9000
	s_mov_b32 s80, 0x1b000
	s_mov_b32 s81, 0x25000
	s_mov_b32 s82, 0x2e000
	s_mov_b32 s83, 0x37000
	s_mov_b32 s84, 0x41000
	s_mov_b32 s85, 0x4a000
	s_mov_b32 s86, 0x53000
	s_mov_b32 s87, 0x5d000
	s_mov_b32 s88, 0x66000
	s_mov_b32 s89, 0x6f000
	s_mov_b32 s90, 0x79000
	s_mov_b32 s91, 0x82000
	s_mov_b32 s92, 0x8b000
	v_add_u32_e32 v100, v6, v7
	v_lshlrev_b32_e32 v78, 1, v2
	v_lshlrev_b32_e32 v82, 2, v0
	v_mov_b32_e32 v101, 0x43e00000
	v_mov_b32_e32 v104, v79
	v_mov_b32_e32 v105, v79
	v_mov_b32_e32 v106, v79
	v_mov_b32_e32 v107, v79
	v_add_u32_e32 v102, v8, v9
	s_branch .LBB0_1062
